# final_kernel: 8 v[] gathers issued together with one wait; scatter_kernel: 16-byte LDS reads and global stores for the copy-out
# speedup vs baseline: 1.0966x; 1.0015x over previous
.LBB0_23:
	s_or_b64 exec, exec, s[4:5]
	v_lshlrev_b32_e32 v15, 4, v0
	s_waitcnt lgkmcnt(0)
	s_barrier
	ds_read_b128 v[16:19], v15 offset:32000
	ds_read_b128 v[20:23], v15 offset:48384
	ds_read_b128 v[24:27], v15 offset:64768
	s_load_dwordx2 s[6:7], s[0:1], 0x38
	s_mul_i32 s4, s2, 0xfa00
	s_mul_hi_i32 s3, s2, 0xfa00
	s_add_u32 s8, s8, s4
	s_addc_u32 s9, s9, s3
	v_add_u32_e32 v28, 0x4000, v15
	v_add_u32_e32 v29, 0x8000, v15
	v_add_u32_e32 v30, 0xc000, v15
	s_movk_i32 s3, 0x3a0
	v_cmp_gt_u32_e64 s[4:5], s3, v0
	s_waitcnt lgkmcnt(0)
	global_store_dwordx4 v15, v[16:19], s[8:9]
	global_store_dwordx4 v28, v[20:23], s[8:9]
	global_store_dwordx4 v29, v[24:27], s[8:9]
	s_and_saveexec_b64 s[10:11], s[4:5]
	s_cbranch_execz .LBB0_25
	ds_read_b128 v[32:35], v30 offset:32000
	s_waitcnt lgkmcnt(0)
	global_store_dwordx4 v30, v[32:35], s[8:9]

.LBB0_27:
	s_or_b64 exec, exec, s[4:5]
	s_waitcnt lgkmcnt(0)
	s_barrier
	v_lshlrev_b32_e32 v15, 4, v0
	ds_read_b128 v[2:5], v15
	s_mul_i32 s4, s2, 0x7d00
	s_mul_hi_i32 s3, s2, 0x7d00
	s_add_u32 s4, s6, s4
	s_addc_u32 s5, s7, s3
	s_movk_i32 s3, 0x3d0
	v_cmp_gt_u32_e32 vcc, s3, v0
	s_waitcnt lgkmcnt(0)
	global_store_dwordx4 v15, v[2:5], s[4:5]
	s_and_saveexec_b64 s[6:7], vcc
	s_cbranch_execz .LBB0_29
	ds_read_b128 v[6:9], v15 offset:16384
	v_add_u32_e32 v16, 0x4000, v15
	s_waitcnt lgkmcnt(0)
	global_store_dwordx4 v16, v[6:9], s[4:5]

.LBB2_4:
	s_or_b64 exec, exec, s[4:5]
	s_load_dwordx2 s[26:27], s[0:1], 0x0
	v_lshlrev_b32_e32 v36, 3, v0
	s_and_saveexec_b64 s[4:5], s[2:3]
	v_mov_b32_e32 v4, 0
	v_mov_b32_e32 v5, v4
	ds_write_b64 v36, v[4:5]
	s_or_b64 exec, exec, s[4:5]
	s_load_dwordx2 s[24:25], s[0:1], 0x10
	v_cmp_eq_u32_e64 s[2:3], 0, v0
	s_and_saveexec_b64 s[4:5], s[2:3]
	v_mov_b32_e32 v4, 0
	ds_write_b32 v4, v4 offset:1568
	s_or_b64 exec, exec, s[4:5]
	v_mul_u32_u24_e32 v26, 0x1f40, v1
	v_mov_b32_e32 v27, 0
	v_max_i32_e32 v1, 1, v35
	v_and_b32_e32 v37, 3, v0
	v_lshl_add_u64 v[2:3], v[2:3], 0, v[26:27]
	v_add_u32_e32 v6, -1, v1
	v_lshlrev_b32_e32 v1, 1, v37
	v_cndmask_b32_e32 v23, 0, v3, vcc
	v_cndmask_b32_e32 v22, 0, v2, vcc
	v_min_u32_e32 v2, v1, v6
	v_or_b32_e32 v30, 8, v1
	s_waitcnt lgkmcnt(0)
	v_lshl_add_u64 v[28:29], v[22:23], 3, s[26:27]
	v_lshlrev_b32_e32 v26, 3, v2
	v_min_u32_e32 v4, v30, v6
	v_lshl_add_u64 v[2:3], v[28:29], 0, v[26:27]
	v_lshlrev_b32_e32 v26, 3, v4
	v_or_b32_e32 v25, 16, v1
	v_lshl_add_u64 v[4:5], v[28:29], 0, v[26:27]
	global_load_dwordx4 v[14:17], v[2:3], off
	global_load_dwordx4 v[10:13], v[4:5], off
	v_min_u32_e32 v2, v25, v6
	v_or_b32_e32 v24, 24, v1
	v_lshlrev_b32_e32 v26, 3, v2
	v_min_u32_e32 v2, v24, v6
	v_lshl_add_u64 v[32:33], v[28:29], 0, v[26:27]
	v_lshlrev_b32_e32 v26, 3, v2
	v_lshl_add_u64 v[38:39], v[28:29], 0, v[26:27]
	global_load_dwordx4 v[6:9], v[32:33], off
	global_load_dwordx4 v[2:5], v[38:39], off
	s_mov_b32 s36, 0x7a120
	v_cmp_lt_i32_e64 s[16:17], v1, v35
	v_or_b32_e32 v40, 1, v1
	v_cmp_lt_i32_e64 s[14:15], v40, v35
	v_cmp_lt_i32_e64 s[12:13], v30, v35
	v_or_b32_e32 v40, 9, v1
	v_cmp_lt_i32_e64 s[10:11], v40, v35
	v_cmp_lt_i32_e64 s[8:9], v25, v35
	v_or_b32_e32 v40, 17, v1
	v_cmp_lt_i32_e64 s[6:7], v40, v35
	v_cmp_lt_i32_e64 s[4:5], v24, v35
	v_or_b32_e32 v1, 25, v1
	v_cmp_lt_i32_e64 s[34:35], v1, v35
	s_waitcnt vmcnt(3)
	v_and_b32_e32 v40, 0x7ffff, v14
	v_cmp_gt_u32_e64 s[30:31], s36, v40
	s_and_b64 s[30:31], s[30:31], s[16:17]
	s_nop 1
	v_cndmask_b32_e64 v40, 0, v40, s[30:31]
	v_lshlrev_b32_e32 v40, 2, v40
	global_load_dword v40, v40, s[24:25]
	v_and_b32_e32 v41, 0x7ffff, v16
	v_cmp_gt_u32_e64 s[30:31], s36, v41
	s_and_b64 s[30:31], s[30:31], s[14:15]
	s_nop 1
	v_cndmask_b32_e64 v41, 0, v41, s[30:31]
	v_lshlrev_b32_e32 v41, 2, v41
	global_load_dword v41, v41, s[24:25]
	s_waitcnt vmcnt(4)
	v_and_b32_e32 v42, 0x7ffff, v10
	v_cmp_gt_u32_e64 s[30:31], s36, v42
	s_and_b64 s[30:31], s[30:31], s[12:13]
	s_nop 1
	v_cndmask_b32_e64 v42, 0, v42, s[30:31]
	v_lshlrev_b32_e32 v42, 2, v42
	global_load_dword v42, v42, s[24:25]
	v_and_b32_e32 v43, 0x7ffff, v12
	v_cmp_gt_u32_e64 s[30:31], s36, v43
	s_and_b64 s[30:31], s[30:31], s[10:11]
	s_nop 1
	v_cndmask_b32_e64 v43, 0, v43, s[30:31]
	v_lshlrev_b32_e32 v43, 2, v43
	global_load_dword v43, v43, s[24:25]
	s_waitcnt vmcnt(5)
	v_and_b32_e32 v44, 0x7ffff, v6
	v_cmp_gt_u32_e64 s[30:31], s36, v44
	s_and_b64 s[30:31], s[30:31], s[8:9]
	s_nop 1
	v_cndmask_b32_e64 v44, 0, v44, s[30:31]
	v_lshlrev_b32_e32 v44, 2, v44
	global_load_dword v44, v44, s[24:25]
	v_and_b32_e32 v45, 0x7ffff, v8
	v_cmp_gt_u32_e64 s[30:31], s36, v45
	s_and_b64 s[30:31], s[30:31], s[6:7]
	s_nop 1
	v_cndmask_b32_e64 v45, 0, v45, s[30:31]
	v_lshlrev_b32_e32 v45, 2, v45
	global_load_dword v45, v45, s[24:25]
	s_waitcnt vmcnt(6)
	v_and_b32_e32 v32, 0x7ffff, v2
	v_cmp_gt_u32_e64 s[30:31], s36, v32
	s_and_b64 s[30:31], s[30:31], s[4:5]
	s_nop 1
	v_cndmask_b32_e64 v32, 0, v32, s[30:31]
	v_lshlrev_b32_e32 v32, 2, v32
	global_load_dword v32, v32, s[24:25]
	v_and_b32_e32 v33, 0x7ffff, v4
	v_cmp_gt_u32_e64 s[30:31], s36, v33
	s_and_b64 s[30:31], s[30:31], s[34:35]
	s_nop 1
	v_cndmask_b32_e64 v33, 0, v33, s[30:31]
	v_lshlrev_b32_e32 v33, 2, v33
	global_load_dword v33, v33, s[24:25]
	s_mov_b64 vcc, s[34:35]
	s_waitcnt vmcnt(0)
	v_mul_f32_e32 v26, v15, v40
	v_mul_f32_e32 v27, v17, v41
	v_mul_f32_e32 v17, v11, v42
	v_mul_f32_e32 v15, v13, v43
	v_mul_f32_e32 v13, v7, v44
	v_mul_f32_e32 v11, v9, v45
	v_mul_f32_e32 v9, v3, v32
	v_mul_f32_e32 v7, v5, v33
	v_cndmask_b32_e64 v26, 0, v26, s[16:17]
	v_cndmask_b32_e64 v27, 0, v27, s[14:15]
	v_cndmask_b32_e64 v17, 0, v17, s[12:13]
	v_cndmask_b32_e64 v15, 0, v15, s[10:11]
	v_cndmask_b32_e64 v13, 0, v13, s[8:9]
	v_cndmask_b32_e64 v11, 0, v11, s[6:7]
	v_cndmask_b32_e64 v9, 0, v9, s[4:5]
	v_cndmask_b32_e64 v7, 0, v7, vcc
.LBB2_24:
	v_max3_f32 v1, |v26|, 0, |v27|
	v_max3_f32 v1, v1, |v17|, |v15|
	v_max3_f32 v1, v1, |v13|, |v11|
	v_or_b32_e32 v24, 32, v37
	v_max3_f32 v1, v1, |v9|, |v7|
	v_cmp_lt_i32_e64 s[2:3], v24, v35
	s_and_saveexec_b64 s[28:29], s[2:3]
	s_cbranch_execz .LBB2_34
	s_waitcnt vmcnt(0)
	v_sub_u32_e32 v3, v35, v37
	v_subrev_u32_e32 v3, 33, v3
	v_cmp_lt_u32_e64 s[18:19], 3, v3
	s_mov_b64 s[34:35], -1
	v_mov_b32_e32 v30, v24
	s_and_saveexec_b64 s[30:31], s[18:19]
	s_cbranch_execz .LBB2_29
	v_lshrrev_b32_e32 v3, 2, v3
	v_add_u32_e32 v3, 1, v3
	v_or_b32_e32 v25, 4, v24
	s_mov_b32 s33, 2
	v_and_b32_e32 v5, 0x7ffffffe, v3
	s_mov_b64 s[36:37], 0
	v_mov_b32_e32 v31, 0
	v_mov_b64_e32 v[32:33], v[24:25]
	v_mov_b32_e32 v25, v1
